# s13
# speedup vs baseline: 1.0080x; 1.0080x over previous
_Z11attn_kernelILi4EEvPKfS1_S1_S1_S1_S1_PKcPf:
	s_load_dwordx2 s[24:25], s[0:1], 0x30
	s_load_dwordx8 s[8:15], s[0:1], 0x0
	s_load_dwordx4 s[16:19], s[0:1], 0x20
	v_lshrrev_b32_e32 v63, 6, v0
	v_and_b32_e32 v57, 15, v0
	v_bfe_u32 v1, v0, 4, 2
	v_lshrrev_b32_e32 v2, 2, v57
	v_mul_u32_u24_e32 v4, 3, v1
	v_mul_u32_u24_e32 v2, 3, v2
	v_mad_u32_u24 v4, v63, 12, v4
	v_mad_u32_u24 v2, v63, 12, v2
	v_lshlrev_b32_e32 v4, 2, v4
	v_lshlrev_b32_e32 v2, 2, v2
	v_and_b32_e32 v104, 63, v0
	v_lshlrev_b32_e32 v60, 5, v57
	v_lshlrev_b32_e32 v58, 3, v1
	v_add_u32_e32 v3, v60, v58
	v_lshrrev_b32_e32 v56, 4, v0
	v_lshlrev_b32_e32 v54, 4, v57
	v_mov_b32_e32 v59, 0
	s_movk_i32 s4, 0xe0
	v_cmp_gt_u32_e64 s[4:5], s4, v0
	s_lshl_b32 s26, s2, 8
	s_lshl_b32 s27, s2, 9
	s_mul_i32 s28, s2, 14
	s_add_u32 s26, s26, 0x164000
	s_add_u32 s27, s27, 0x80000
	s_add_u32 s20, s26, 0xc0
	v_lshlrev_b32_e32 v5, 2, v57
	v_lshlrev_b32_e32 v147, 6, v57
	v_add_u32_e32 v2, s26, v2
	v_add_u32_e32 v4, s26, v4
	v_add_u32_e32 v3, s27, v3
	v_mul_u32_u24_e32 v156, 0x140, v1
	s_movk_i32 s21, 0x500
	v_mad_u32_u24 v156, v63, s21, v156
	v_lshl_or_b32 v156, v57, 2, v156
	v_add_u32_e32 v156, 0x1c00, v156
	v_lshlrev_b32_e32 v157, 5, v56
	v_cmp_gt_u32_e32 vcc, 3, v57
	v_add_u32_e32 v158, 4, v57
	v_lshlrev_b32_e32 v159, 2, v57
	s_movk_i32 s21, 0x50
	v_cndmask_b32_e32 v158, 4, v158, vcc
	v_mad_u32_u24 v159, v56, s21, v159
	v_lshl_add_u32 v158, v158, 2, v157
	v_mul_u32_u24_e32 v250, 0x50, v56
	v_or_b32_e32 v250, 0x3800, v250
	v_lshl_add_u32 v251, v57, 1, v250
	v_mul_u32_u24_e32 v252, 0x50, v57
	v_lshl_add_u32 v252, v58, 1, v252
	v_lshlrev_b32_e32 v253, 2, v57
	v_and_b32_e32 v254, 0xc0, v0
	v_lshlrev_b32_e32 v255, 11, v1
	v_or3_b32 v253, v253, v254, v255
	v_add_u32_e32 v254, s28, v56
	v_lshl_add_u32 v254, v254, 9, v54
	v_lshl_or_b32 v255, v56, 9, v54
	s_waitcnt lgkmcnt(0)
	global_load_dwordx3 v[80:82], v2, s[24:25]
	global_load_dwordx3 v[84:86], v4, s[24:25]
	global_load_dwordx2 v[64:65], v3, s[24:25]
	s_load_dword s3, s[24:25], s20
	s_add_u32 s22, s24, 0x160000
	s_addc_u32 s23, s25, 0
	v_cndmask_b32_e64 v62, 13, v56, s[4:5]
	v_add_u32_e32 v3, s28, v62
	v_mad_u32_u24 v144, v3, 36, v5
	v_mad_u32_u24 v146, v3, 12, v5
	v_add_u32_e32 v145, -36, v146
	v_add_u32_e32 v146, -48, v146
	v_lshl_or_b32 v147, v63, 10, v147
	v_lshl_or_b32 v147, v1, 4, v147
	v_or_b32_e32 v148, 0x1000, v147
	v_lshlrev_b32_e32 v149, 4, v104
	v_lshlrev_b32_e32 v150, 9, v3
	v_add_u32_e32 v150, v150, v54
	v_and_b32_e32 v87, 3, v57
	v_lshlrev_b32_e32 v87, 4, v87
	v_lshl_or_b32 v87, v1, 6, v87
	v_lshlrev_b32_e32 v88, 3, v57
	s_add_u32 s26, s24, 0x100000
	s_addc_u32 s27, s25, 0
	s_add_u32 s28, s24, 0x140000
	s_addc_u32 s29, s25, 0
	s_waitcnt lgkmcnt(0)
	s_bitcmp0_b32 s3, 1
	s_cselect_b64 s[20:21], -1, 0
	s_cbranch_scc1 .LBB1_16
	s_waitcnt vmcnt(1)
	v_lshl_add_u32 v72, v80, 9, v87
	v_lshl_add_u32 v73, v81, 9, v87
	v_lshl_add_u32 v74, v82, 9, v87
	global_load_dwordx4 v[50:53], v72, s[24:25]
	global_load_dwordx4 v[46:49], v72, s[24:25] offset:256
	global_load_dwordx4 v[14:17], v73, s[24:25]
	global_load_dwordx4 v[10:13], v73, s[24:25] offset:256
	global_load_dwordx4 v[6:9], v74, s[24:25]
	global_load_dwordx4 v[2:5], v74, s[24:25] offset:256
	v_lshl_add_u32 v75, v84, 8, v54
	v_lshl_add_u32 v78, v84, 7, v88
	v_lshl_add_u32 v76, v85, 8, v54
	v_lshl_add_u32 v79, v85, 7, v88
	v_lshl_add_u32 v77, v86, 8, v54
	v_lshl_add_u32 v80, v86, 7, v88
	global_load_dwordx4 v[30:33], v75, s[26:27]
	global_load_dwordx2 v[70:71], v78, s[28:29]
	global_load_dwordx4 v[26:29], v76, s[26:27]
	global_load_dwordx2 v[66:67], v79, s[28:29]
	global_load_dwordx4 v[18:21], v77, s[26:27]
	global_load_dwordx2 v[68:69], v80, s[28:29]
	s_mov_b32 exec_lo, 0x1ff01ff
	s_mov_b32 exec_hi, 0x1ff01ff
	global_load_dword v120, v144, s[10:11]
	s_mov_b32 exec_lo, 0xe000e00
	s_mov_b32 exec_hi, 0xe000e00
	global_load_dword v120, v145, s[12:13]
	s_mov_b32 exec_lo, 0x70007000
	s_mov_b32 exec_hi, 0x70007000
	global_load_dword v120, v146, s[14:15]
	s_mov_b64 exec, -1
	global_load_dwordx4 v[124:127], v147, s[22:23]
	global_load_dwordx4 v[128:131], v148, s[22:23]
	s_mov_b32 exec_hi, 0
	global_load_dwordx4 v[132:135], v149, s[16:17]
	s_mov_b32 exec_hi, -1
	s_mov_b32 exec_lo, 0
	global_load_dwordx4 v[132:135], v149, s[18:19] offset:-512
	s_mov_b32 exec_lo, -1
	global_load_dwordx4 v[136:139], v150, s[8:9]
	global_load_dwordx4 v[140:143], v150, s[8:9] offset:256
	s_movk_i32 s6, 0x140
	v_cmp_gt_u32_e32 vcc, s6, v0
	v_lshlrev_b32_e32 v22, 2, v0
	v_mov_b32_e32 v23, 0
	s_and_saveexec_b64 s[6:7], vcc
	ds_write_b32 v22, v23 offset:14336
	s_or_b64 exec, exec, s[6:7]
	v_cmp_gt_u32_e32 vcc, 64, v0
	s_and_saveexec_b64 s[6:7], vcc
	ds_write_b32 v22, v23 offset:15360
	s_or_b64 exec, exec, s[6:7]
	v_bfe_u32 v22, s3, v57, 1
	v_cmp_eq_u32_e32 vcc, 0, v22
	v_mov_b32_e32 v45, 0xc9c35000
	s_mov_b32 s30, 0x3db8aa3b
	s_mov_b32 s31, 0x3db8aa3b
	v_cndmask_b32_e64 v55, 1.0, 0, vcc
	v_mov_b32_e32 v121, 0x3fb8aa3b
	s_bitcmp0_b32 s3, 0
	s_cselect_b64 vcc, -1, 0
	v_cndmask_b32_e32 v34, 0, v45, vcc
	s_bitcmp0_b32 s3, 2
	s_cselect_b64 vcc, -1, 0
	v_cndmask_b32_e32 v36, 0, v45, vcc
	s_bitcmp0_b32 s3, 3
	s_cselect_b64 vcc, -1, 0
	v_cndmask_b32_e32 v37, 0, v45, vcc
	s_bitcmp0_b32 s3, 4
	s_cselect_b64 vcc, -1, 0
	v_cndmask_b32_e32 v22, 0, v45, vcc
	s_bitcmp0_b32 s3, 5
	s_cselect_b64 vcc, -1, 0
	v_cndmask_b32_e32 v23, 0, v45, vcc
	s_bitcmp0_b32 s3, 6
	s_cselect_b64 vcc, -1, 0
	v_cndmask_b32_e32 v24, 0, v45, vcc
	s_bitcmp0_b32 s3, 7
	s_cselect_b64 vcc, -1, 0
	v_cndmask_b32_e32 v25, 0, v45, vcc
	s_bitcmp0_b32 s3, 8
	s_cselect_b64 vcc, -1, 0
	v_cndmask_b32_e32 v38, 0, v45, vcc
	s_bitcmp0_b32 s3, 9
	s_cselect_b64 vcc, -1, 0
	v_cndmask_b32_e32 v39, 0, v45, vcc
	s_bitcmp0_b32 s3, 10
	s_cselect_b64 vcc, -1, 0
	v_cndmask_b32_e32 v40, 0, v45, vcc
	s_bitcmp0_b32 s3, 11
	s_cselect_b64 vcc, -1, 0
	v_cndmask_b32_e32 v41, 0, v45, vcc
	s_bitcmp0_b32 s3, 12
	s_cselect_b64 vcc, -1, 0
	v_cndmask_b32_e32 v42, 0, v45, vcc
	s_bitcmp0_b32 s3, 13
	s_cselect_b64 vcc, -1, 0
	v_cndmask_b32_e32 v43, 0, v45, vcc
	v_mov_b32_e32 v35, 0
	v_mov_b32_e32 v44, v45
	v_mov_b32_e32 v75, 0
	v_mov_b32_e32 v79, 0
	v_mov_b32_e32 v83, 0
	s_waitcnt vmcnt(20)
	v_mfma_f32_16x16x32_fp8_fp8 v[160:163], v[50:51], v[64:65], v[34:37]
	v_mfma_f32_16x16x32_fp8_fp8 v[164:167], v[52:53], v[64:65], v[22:25]
	s_waitcnt vmcnt(19)
	v_mfma_f32_16x16x32_fp8_fp8 v[168:171], v[46:47], v[64:65], v[38:41]
	v_mfma_f32_16x16x32_fp8_fp8 v[172:175], v[48:49], v[64:65], v[42:45]
	s_nop 3
	v_max3_f32 v86, v160, v161, v162
	v_max3_f32 v87, v163, v164, v165
	v_max3_f32 v88, v166, v167, v168
	v_max3_f32 v89, v169, v170, v171
	v_max3_f32 v86, v86, v172, v173
	v_max3_f32 v87, v87, v88, v89
	v_max_f32_e32 v96, v86, v87
	v_mul_f32_e32 v98, 0xbdb8aa3b, v96
	v_pk_fma_f32 v[208:209], v[160:161], s[30:31], v[98:99] op_sel_hi:[1,1,0]
	v_pk_fma_f32 v[210:211], v[162:163], s[30:31], v[98:99] op_sel_hi:[1,1,0]
	v_pk_fma_f32 v[212:213], v[164:165], s[30:31], v[98:99] op_sel_hi:[1,1,0]
	v_pk_fma_f32 v[214:215], v[166:167], s[30:31], v[98:99] op_sel_hi:[1,1,0]
	v_pk_fma_f32 v[216:217], v[168:169], s[30:31], v[98:99] op_sel_hi:[1,1,0]
	v_pk_fma_f32 v[218:219], v[170:171], s[30:31], v[98:99] op_sel_hi:[1,1,0]
	v_pk_fma_f32 v[220:221], v[172:173], s[30:31], v[98:99] op_sel_hi:[1,1,0]
	v_exp_f32_e32 v208, v208
	v_exp_f32_e32 v209, v209
	v_exp_f32_e32 v210, v210
	v_exp_f32_e32 v211, v211
	v_exp_f32_e32 v212, v212
	v_exp_f32_e32 v213, v213
	v_exp_f32_e32 v214, v214
	v_exp_f32_e32 v215, v215
	v_exp_f32_e32 v216, v216
	v_exp_f32_e32 v217, v217
	v_exp_f32_e32 v218, v218
	v_exp_f32_e32 v219, v219
	v_exp_f32_e32 v220, v220
	v_exp_f32_e32 v221, v221
	s_waitcnt vmcnt(18)
	v_mfma_f32_16x16x32_fp8_fp8 v[176:179], v[14:15], v[64:65], v[34:37]
	v_mfma_f32_16x16x32_fp8_fp8 v[180:183], v[16:17], v[64:65], v[22:25]
	s_waitcnt vmcnt(17)
	v_mfma_f32_16x16x32_fp8_fp8 v[184:187], v[10:11], v[64:65], v[38:41]
	v_mfma_f32_16x16x32_fp8_fp8 v[188:191], v[12:13], v[64:65], v[42:45]
	v_pk_add_f32 v[86:87], v[208:209], v[210:211]
	v_pk_add_f32 v[88:89], v[212:213], v[214:215]
	v_pk_add_f32 v[90:91], v[216:217], v[218:219]
	v_pk_mul_f32 v[92:93], v[208:209], v[160:161]
	v_pk_mul_f32 v[94:95], v[210:211], v[162:163]
	v_pk_add_f32 v[86:87], v[86:87], v[220:221]
	v_pk_add_f32 v[88:89], v[88:89], v[90:91]
	v_pk_fma_f32 v[92:93], v[212:213], v[164:165], v[92:93]
	v_pk_fma_f32 v[94:95], v[214:215], v[166:167], v[94:95]
	v_pk_add_f32 v[86:87], v[86:87], v[88:89]
	v_pk_fma_f32 v[92:93], v[216:217], v[168:169], v[92:93]
	v_pk_fma_f32 v[94:95], v[218:219], v[170:171], v[94:95]
	v_add_f32_e32 v86, v86, v87
	v_pk_fma_f32 v[92:93], v[220:221], v[172:173], v[92:93]
	v_rcp_f32_e32 v87, v86
	v_pk_add_f32 v[92:93], v[92:93], v[94:95]
	v_mul_f32_e32 v87, v55, v87
	v_add_f32_e32 v92, v92, v93
	v_mul_f32_e32 v107, v86, v87
	v_mul_f32_e32 v92, v92, v87
	v_mul_f32_e32 v100, 0x43800000, v87
	v_mul_f32_e32 v103, 0x3d800000, v92
	v_max3_f32 v86, v176, v177, v178
	v_max3_f32 v87, v179, v180, v181
	v_max3_f32 v88, v182, v183, v184
	v_max3_f32 v89, v185, v186, v187
	v_max3_f32 v86, v86, v188, v189
	v_max3_f32 v87, v87, v88, v89
	v_max_f32_e32 v96, v86, v87
	v_mul_f32_e32 v98, 0xbdb8aa3b, v96
	v_pk_fma_f32 v[222:223], v[176:177], s[30:31], v[98:99] op_sel_hi:[1,1,0]
	v_pk_fma_f32 v[224:225], v[178:179], s[30:31], v[98:99] op_sel_hi:[1,1,0]
	v_pk_fma_f32 v[226:227], v[180:181], s[30:31], v[98:99] op_sel_hi:[1,1,0]
	v_pk_fma_f32 v[228:229], v[182:183], s[30:31], v[98:99] op_sel_hi:[1,1,0]
	v_pk_fma_f32 v[230:231], v[184:185], s[30:31], v[98:99] op_sel_hi:[1,1,0]
	v_pk_fma_f32 v[232:233], v[186:187], s[30:31], v[98:99] op_sel_hi:[1,1,0]
	v_pk_fma_f32 v[234:235], v[188:189], s[30:31], v[98:99] op_sel_hi:[1,1,0]
	v_exp_f32_e32 v222, v222
	v_exp_f32_e32 v223, v223
	v_exp_f32_e32 v224, v224
	v_exp_f32_e32 v225, v225
	v_exp_f32_e32 v226, v226
	v_exp_f32_e32 v227, v227
	v_exp_f32_e32 v228, v228
	v_exp_f32_e32 v229, v229
	v_exp_f32_e32 v230, v230
	v_exp_f32_e32 v231, v231
	v_exp_f32_e32 v232, v232
	v_exp_f32_e32 v233, v233
	v_exp_f32_e32 v234, v234
	v_exp_f32_e32 v235, v235
	s_waitcnt vmcnt(16)
	v_mfma_f32_16x16x32_fp8_fp8 v[192:195], v[6:7], v[64:65], v[34:37]
	v_mfma_f32_16x16x32_fp8_fp8 v[196:199], v[8:9], v[64:65], v[22:25]
	s_waitcnt vmcnt(15)
	v_mfma_f32_16x16x32_fp8_fp8 v[200:203], v[2:3], v[64:65], v[38:41]
	v_mfma_f32_16x16x32_fp8_fp8 v[204:207], v[4:5], v[64:65], v[42:45]
	v_pk_add_f32 v[86:87], v[222:223], v[224:225]
	v_pk_add_f32 v[88:89], v[226:227], v[228:229]
	v_pk_add_f32 v[90:91], v[230:231], v[232:233]
	v_pk_mul_f32 v[92:93], v[222:223], v[176:177]
	v_pk_mul_f32 v[94:95], v[224:225], v[178:179]
	v_pk_add_f32 v[86:87], v[86:87], v[234:235]
	v_pk_add_f32 v[88:89], v[88:89], v[90:91]
	v_pk_fma_f32 v[92:93], v[226:227], v[180:181], v[92:93]
	v_pk_fma_f32 v[94:95], v[228:229], v[182:183], v[94:95]
	v_pk_add_f32 v[86:87], v[86:87], v[88:89]
	v_pk_fma_f32 v[92:93], v[230:231], v[184:185], v[92:93]
	v_pk_fma_f32 v[94:95], v[232:233], v[186:187], v[94:95]
	v_add_f32_e32 v86, v86, v87
	v_pk_fma_f32 v[92:93], v[234:235], v[188:189], v[92:93]
	v_rcp_f32_e32 v87, v86
	v_pk_add_f32 v[92:93], v[92:93], v[94:95]
	v_mul_f32_e32 v87, v55, v87
	v_add_f32_e32 v92, v92, v93
	v_mul_f32_e32 v108, v86, v87
	v_mul_f32_e32 v92, v92, v87
	v_mul_f32_e32 v101, 0x43800000, v87
	v_mul_f32_e32 v105, 0x3d800000, v92
	v_max3_f32 v86, v192, v193, v194
	v_max3_f32 v87, v195, v196, v197
	v_max3_f32 v88, v198, v199, v200
	v_max3_f32 v89, v201, v202, v203
	v_max3_f32 v86, v86, v204, v205
	v_max3_f32 v87, v87, v88, v89
	v_max_f32_e32 v96, v86, v87
	v_mul_f32_e32 v98, 0xbdb8aa3b, v96
	v_pk_fma_f32 v[236:237], v[192:193], s[30:31], v[98:99] op_sel_hi:[1,1,0]
	v_pk_fma_f32 v[238:239], v[194:195], s[30:31], v[98:99] op_sel_hi:[1,1,0]
	v_pk_fma_f32 v[240:241], v[196:197], s[30:31], v[98:99] op_sel_hi:[1,1,0]
	v_pk_fma_f32 v[242:243], v[198:199], s[30:31], v[98:99] op_sel_hi:[1,1,0]
	v_pk_fma_f32 v[244:245], v[200:201], s[30:31], v[98:99] op_sel_hi:[1,1,0]
	v_pk_fma_f32 v[246:247], v[202:203], s[30:31], v[98:99] op_sel_hi:[1,1,0]
	v_pk_fma_f32 v[248:249], v[204:205], s[30:31], v[98:99] op_sel_hi:[1,1,0]
	v_exp_f32_e32 v236, v236
	v_exp_f32_e32 v237, v237
	v_exp_f32_e32 v238, v238
	v_exp_f32_e32 v239, v239
	v_exp_f32_e32 v240, v240
	v_exp_f32_e32 v241, v241
	v_exp_f32_e32 v242, v242
	v_exp_f32_e32 v243, v243
	v_exp_f32_e32 v244, v244
	v_exp_f32_e32 v245, v245
	v_exp_f32_e32 v246, v246
	v_exp_f32_e32 v247, v247
	v_exp_f32_e32 v248, v248
	v_exp_f32_e32 v249, v249
	v_pk_add_f32 v[86:87], v[236:237], v[238:239]
	v_pk_add_f32 v[88:89], v[240:241], v[242:243]
	v_pk_add_f32 v[90:91], v[244:245], v[246:247]
	v_pk_mul_f32 v[92:93], v[236:237], v[192:193]
	v_pk_mul_f32 v[94:95], v[238:239], v[194:195]
	v_pk_add_f32 v[86:87], v[86:87], v[248:249]
	v_pk_add_f32 v[88:89], v[88:89], v[90:91]
	v_pk_fma_f32 v[92:93], v[240:241], v[196:197], v[92:93]
	v_pk_fma_f32 v[94:95], v[242:243], v[198:199], v[94:95]
	v_pk_add_f32 v[86:87], v[86:87], v[88:89]
	v_pk_fma_f32 v[92:93], v[244:245], v[200:201], v[92:93]
	v_pk_fma_f32 v[94:95], v[246:247], v[202:203], v[94:95]
	v_add_f32_e32 v86, v86, v87
	v_pk_fma_f32 v[92:93], v[248:249], v[204:205], v[92:93]
	v_rcp_f32_e32 v87, v86
	v_pk_add_f32 v[92:93], v[92:93], v[94:95]
	v_mul_f32_e32 v87, v55, v87
	v_add_f32_e32 v92, v92, v93
	v_mul_f32_e32 v109, v86, v87
	v_mul_f32_e32 v92, v92, v87
	v_mul_f32_e32 v102, 0x43800000, v87
	v_mul_f32_e32 v106, 0x3d800000, v92
	v_max3_f32 v122, v103, v105, v106
	v_cmp_gt_u32_e64 s[6:7], 16, v104
	v_mov_b32_e32 v123, v122
	s_nop 1
	v_permlane16_swap_b32_e32 v122, v123
	v_max_f32_e32 v122, v122, v123
	v_mov_b32_e32 v123, v122
	s_nop 1
	v_permlane32_swap_b32_e32 v122, v123
	v_max_f32_e32 v36, v122, v123
	v_mul_f32_e32 v123, 0x3fb8aa3b, v36
	v_fma_f32 v111, v103, v121, -v123
	v_exp_f32_e32 v111, v111
	s_nop 0
	v_mul_f32_e32 v112, v111, v100
	v_mul_f32_e32 v110, v111, v107
	v_mov_b32_e32 v114, v111
	v_pk_mul_f32 v[208:209], v[208:209], v[112:113] op_sel_hi:[1,0]
	v_pk_mul_f32 v[210:211], v[210:211], v[112:113] op_sel_hi:[1,0]
	v_pk_mul_f32 v[212:213], v[212:213], v[112:113] op_sel_hi:[1,0]
	v_pk_mul_f32 v[214:215], v[214:215], v[112:113] op_sel_hi:[1,0]
	v_pk_mul_f32 v[216:217], v[216:217], v[112:113] op_sel_hi:[1,0]
	v_pk_mul_f32 v[218:219], v[218:219], v[112:113] op_sel_hi:[1,0]
	v_pk_mul_f32 v[220:221], v[220:221], v[112:113] op_sel_hi:[1,0]
	s_waitcnt vmcnt(13)
	v_mov_b32_e32 v115, v110
	v_fma_mix_f32 v116, v110, v70, 0 op_sel_hi:[0,1,0]
	v_fma_mix_f32 v117, v110, v70, 0 op_sel:[0,1,0] op_sel_hi:[0,1,0]
	v_fma_mix_f32 v118, v110, v71, 0 op_sel_hi:[0,1,0]
	v_cvt_pk_fp8_f32 v72, v208, v209
	v_cvt_pk_fp8_f32 v73, v212, v213
	v_cvt_pk_fp8_f32 v74, v216, v217
	v_cvt_pk_fp8_f32 v75, v220, v221
	v_cvt_pk_fp8_f32 v72, v210, v211 op_sel:[0,0,1]
	v_cvt_pk_fp8_f32 v73, v214, v215 op_sel:[0,0,1]
	v_cvt_pk_fp8_f32 v74, v218, v219 op_sel:[0,0,1]
	s_nop 1
	v_mfma_f32_16x16x32_fp8_fp8 v[152:155], v[72:73], v[30:31], 0
	v_mfma_f32_16x16x32_fp8_fp8 v[152:155], v[74:75], v[32:33], v[152:155]
	v_fma_f32 v111, v105, v121, -v123
	v_exp_f32_e32 v111, v111
	s_nop 0
	v_mul_f32_e32 v112, v111, v101
	v_mul_f32_e32 v110, v111, v108
	v_add_f32_e32 v114, v114, v111
	v_pk_mul_f32 v[222:223], v[222:223], v[112:113] op_sel_hi:[1,0]
	v_pk_mul_f32 v[224:225], v[224:225], v[112:113] op_sel_hi:[1,0]
	v_pk_mul_f32 v[226:227], v[226:227], v[112:113] op_sel_hi:[1,0]
	v_pk_mul_f32 v[228:229], v[228:229], v[112:113] op_sel_hi:[1,0]
	v_pk_mul_f32 v[230:231], v[230:231], v[112:113] op_sel_hi:[1,0]
	v_pk_mul_f32 v[232:233], v[232:233], v[112:113] op_sel_hi:[1,0]
	v_pk_mul_f32 v[234:235], v[234:235], v[112:113] op_sel_hi:[1,0]
	s_waitcnt vmcnt(11)
	v_add_f32_e32 v115, v115, v110
	v_fma_mix_f32 v116, v110, v66, v116 op_sel_hi:[0,1,0]
	v_fma_mix_f32 v117, v110, v66, v117 op_sel:[0,1,0] op_sel_hi:[0,1,0]
	v_fma_mix_f32 v118, v110, v67, v118 op_sel_hi:[0,1,0]
	v_cvt_pk_fp8_f32 v76, v222, v223
	v_cvt_pk_fp8_f32 v77, v226, v227
	v_cvt_pk_fp8_f32 v78, v230, v231
	v_cvt_pk_fp8_f32 v79, v234, v235
	v_cvt_pk_fp8_f32 v76, v224, v225 op_sel:[0,0,1]
	v_cvt_pk_fp8_f32 v77, v228, v229 op_sel:[0,0,1]
	v_cvt_pk_fp8_f32 v78, v232, v233 op_sel:[0,0,1]
	s_nop 1
	v_mfma_f32_16x16x32_fp8_fp8 v[152:155], v[76:77], v[26:27], v[152:155]
	v_mfma_f32_16x16x32_fp8_fp8 v[152:155], v[78:79], v[28:29], v[152:155]
	v_fma_f32 v111, v106, v121, -v123
	v_exp_f32_e32 v111, v111
	s_nop 0
	v_mul_f32_e32 v112, v111, v102
	v_mul_f32_e32 v110, v111, v109
	v_add_f32_e32 v114, v114, v111
	v_pk_mul_f32 v[236:237], v[236:237], v[112:113] op_sel_hi:[1,0]
	v_pk_mul_f32 v[238:239], v[238:239], v[112:113] op_sel_hi:[1,0]
	v_pk_mul_f32 v[240:241], v[240:241], v[112:113] op_sel_hi:[1,0]
	v_pk_mul_f32 v[242:243], v[242:243], v[112:113] op_sel_hi:[1,0]
	v_pk_mul_f32 v[244:245], v[244:245], v[112:113] op_sel_hi:[1,0]
	v_pk_mul_f32 v[246:247], v[246:247], v[112:113] op_sel_hi:[1,0]
	v_pk_mul_f32 v[248:249], v[248:249], v[112:113] op_sel_hi:[1,0]
	s_waitcnt vmcnt(9)
	v_add_f32_e32 v115, v115, v110
	v_fma_mix_f32 v116, v110, v68, v116 op_sel_hi:[0,1,0]
	v_fma_mix_f32 v117, v110, v68, v117 op_sel:[0,1,0] op_sel_hi:[0,1,0]
	v_fma_mix_f32 v118, v110, v69, v118 op_sel_hi:[0,1,0]
	v_cvt_pk_fp8_f32 v80, v236, v237
	v_cvt_pk_fp8_f32 v81, v240, v241
	v_cvt_pk_fp8_f32 v82, v244, v245
	v_cvt_pk_fp8_f32 v83, v248, v249
	v_cvt_pk_fp8_f32 v80, v238, v239 op_sel:[0,0,1]
	v_cvt_pk_fp8_f32 v81, v242, v243 op_sel:[0,0,1]
	v_cvt_pk_fp8_f32 v82, v246, v247 op_sel:[0,0,1]
	s_nop 1
	v_mfma_f32_16x16x32_fp8_fp8 v[152:155], v[80:81], v[18:19], v[152:155]
	v_mfma_f32_16x16x32_fp8_fp8 v[152:155], v[82:83], v[20:21], v[152:155]
	v_mov_b32_e32 v86, v114
	v_mov_b32_e32 v87, v115
	v_mov_b32_e32 v88, v116
	v_mov_b32_e32 v89, v117
	v_mov_b32_e32 v90, v118
	v_permlane16_swap_b32_e32 v114, v86
	v_permlane16_swap_b32_e32 v115, v87
	v_permlane16_swap_b32_e32 v116, v88
	v_permlane16_swap_b32_e32 v117, v89
	v_permlane16_swap_b32_e32 v118, v90
	v_add_f32_e32 v114, v114, v86
	v_add_f32_e32 v115, v115, v87
	v_add_f32_e32 v116, v116, v88
	v_add_f32_e32 v117, v117, v89
	v_add_f32_e32 v118, v118, v90
	v_mov_b32_e32 v86, v114
	v_mov_b32_e32 v87, v115
	v_mov_b32_e32 v88, v116
	v_mov_b32_e32 v89, v117
	v_mov_b32_e32 v90, v118
	v_permlane32_swap_b32_e32 v114, v86
	v_permlane32_swap_b32_e32 v115, v87
	v_permlane32_swap_b32_e32 v116, v88
	v_permlane32_swap_b32_e32 v117, v89
	v_permlane32_swap_b32_e32 v118, v90
	v_add_f32_e32 v37, v114, v86
	v_add_f32_e32 v20, v115, v87
	v_add_f32_e32 v18, v116, v88
	v_add_f32_e32 v19, v117, v89
	v_add_f32_e32 v21, v118, v90
	ds_write2_b32 v156, v152, v153 offset0:0 offset1:20
	ds_write2_b32 v156, v154, v155 offset0:40 offset1:60
	s_branch .LBB1_30
.LBB1_16:
	s_mov_b32 exec_lo, 0x1ff01ff
	s_mov_b32 exec_hi, 0x1ff01ff
	global_load_dword v120, v144, s[10:11]
	s_mov_b32 exec_lo, 0xe000e00
	s_mov_b32 exec_hi, 0xe000e00
	global_load_dword v120, v145, s[12:13]
	s_mov_b32 exec_lo, 0x70007000
	s_mov_b32 exec_hi, 0x70007000
	global_load_dword v120, v146, s[14:15]
	s_mov_b64 exec, -1
	global_load_dwordx4 v[124:127], v147, s[22:23]
	global_load_dwordx4 v[128:131], v148, s[22:23]
	s_mov_b32 exec_hi, 0
	global_load_dwordx4 v[132:135], v149, s[16:17]
	s_mov_b32 exec_hi, -1
	s_mov_b32 exec_lo, 0
	global_load_dwordx4 v[132:135], v149, s[18:19] offset:-512
	s_mov_b32 exec_lo, -1
	global_load_dwordx4 v[136:139], v150, s[8:9]
	global_load_dwordx4 v[140:143], v150, s[8:9] offset:256
	s_movk_i32 s6, 0x140
	v_cmp_gt_u32_e32 vcc, s6, v0
	v_lshlrev_b32_e32 v18, 2, v0
	v_mov_b32_e32 v19, 0
	s_and_saveexec_b64 s[6:7], vcc
	ds_write_b32 v18, v19 offset:14336
	s_or_b64 exec, exec, s[6:7]
	v_cmp_gt_u32_e32 vcc, 64, v0
	s_and_saveexec_b64 s[6:7], vcc
	ds_write_b32 v18, v19 offset:15360
	s_or_b64 exec, exec, s[6:7]
	v_mov_b32_e32 v21, 0
	ds_write2_b32 v156, v21, v21 offset1:20
	ds_write2_b32 v156, v21, v21 offset0:40 offset1:60
	v_cmp_gt_u32_e64 s[6:7], 16, v104
	v_mov_b32_e32 v37, 1.0
	v_mov_b32_e32 v20, 0
	v_mov_b32_e32 v19, 0
	v_mov_b32_e32 v18, 0
	v_mov_b32_e32 v36, 0

.LBB1_32:
	s_or_b64 exec, exec, s[8:9]
	s_movk_i32 s6, 0x100
	v_cmp_gt_u32_e64 s[6:7], s6, v0
	s_waitcnt lgkmcnt(0)
	s_barrier
	s_and_saveexec_b64 s[14:15], s[6:7]
	s_cbranch_execz .LBB1_39
	ds_read_b96 v[160:162], v157 offset:12288
	ds_read_b96 v[164:166], v157 offset:12800
	ds_read_b96 v[168:170], v157 offset:13312
	ds_read_b96 v[172:174], v157 offset:13824
	ds_read2st64_b32 v[176:177], v158 offset0:48 offset1:50
	ds_read2st64_b32 v[178:179], v158 offset0:52 offset1:54
	ds_read2st64_b32 v[180:181], v159 offset0:28 offset1:33
	ds_read2st64_b32 v[182:183], v159 offset0:38 offset1:43
	v_cmp_gt_u32_e32 vcc, 3, v57
	v_cndmask_b32_e64 v18, 1.0, 0, s[20:21]
	s_waitcnt lgkmcnt(4)
	v_max_f32_e32 v21, v160, v164
	v_max3_f32 v33, v21, v168, v172
	v_sub_f32_e32 v21, v160, v33
	v_sub_f32_e32 v29, v164, v33
	v_sub_f32_e32 v30, v168, v33
	v_sub_f32_e32 v33, v172, v33
	v_mul_f32_e32 v21, 0x3fb8aa3b, v21
	v_mul_f32_e32 v29, 0x3fb8aa3b, v29
	v_mul_f32_e32 v30, 0x3fb8aa3b, v30
	v_mul_f32_e32 v33, 0x3fb8aa3b, v33
	v_exp_f32_e32 v21, v21
	v_exp_f32_e32 v29, v29
	v_exp_f32_e32 v30, v30
	v_exp_f32_e32 v33, v33
	v_mov_b32_e32 v20, v250
	v_mul_f32_e32 v35, v21, v161
	v_mul_f32_e32 v34, v21, v162
	v_fmac_f32_e32 v35, v29, v165
	v_fmac_f32_e32 v34, v29, v166
	v_fmac_f32_e32 v35, v30, v169
	v_fmac_f32_e32 v34, v30, v170
	v_fmac_f32_e32 v35, v33, v173
	v_fmac_f32_e32 v34, v33, v174
	v_rcp_f32_e32 v35, v35
	s_waitcnt lgkmcnt(0)
	v_mul_f32_e32 v31, v21, v180
	v_mul_f32_e32 v18, v18, v35
	v_fmac_f32_e32 v31, v29, v181
	v_mul_f32_e32 v35, v21, v176
	v_fmac_f32_e32 v31, v30, v182
	v_fmac_f32_e32 v35, v29, v177
	v_fmac_f32_e32 v31, v33, v183
	v_fmac_f32_e32 v35, v30, v178
	v_mul_f32_e32 v31, v31, v18
	v_fmac_f32_e32 v35, v33, v179
	s_mov_b32 s8, 0x3a800000
	v_fma_mixlo_f16 v31, v31, s8, 0
	v_cmp_eq_u32_e64 s[8:9], 7, v57
	s_and_saveexec_b64 s[10:11], s[4:5]
	ds_write_b16 v251, v31
	s_and_b64 exec, exec, s[8:9]
	v_mov_b32_e32 v31, 0x3c00
	ds_write_b16 v20, v31 offset:46
	s_or_b64 exec, exec, s[10:11]
	s_waitcnt vmcnt(6)
	v_mov_b32_dpp v33, v120 row_newbcast:10 row_mask:0xf bank_mask:0xf bound_ctrl:1
	v_mov_b32_dpp v36, v120 row_newbcast:11 row_mask:0xf bank_mask:0xf bound_ctrl:1
	v_cmp_eq_u32_e64 s[10:11], 1, v57
	v_mov_b32_dpp v32, v120 row_newbcast:9 row_mask:0xf bank_mask:0xf bound_ctrl:1
	v_mov_b32_dpp v38, v120 row_newbcast:13 row_mask:0xf bank_mask:0xf bound_ctrl:1
	v_mov_b32_dpp v39, v120 row_newbcast:14 row_mask:0xf bank_mask:0xf bound_ctrl:1
	v_cndmask_b32_e64 v33, v36, v33, s[10:11]
	v_cmp_eq_u32_e64 s[8:9], 0, v57
	v_mov_b32_dpp v37, v120 row_newbcast:12 row_mask:0xf bank_mask:0xf bound_ctrl:1
	v_mov_b32_dpp v27, v120 row_newbcast:0 row_mask:0xf bank_mask:0xf bound_ctrl:1
	v_cndmask_b32_e64 v32, v33, v32, s[8:9]
	v_cndmask_b32_e64 v33, v39, v38, s[10:11]
	v_cndmask_b32_e64 v33, v33, v37, s[8:9]
	v_fma_f32 v33, v34, v33, -v35
	v_fma_f32 v32, v18, v33, -v32
	v_mov_b32_dpp v20, v120 row_newbcast:1 row_mask:0xf bank_mask:0xf bound_ctrl:1
	v_mov_b32_dpp v19, v120 row_newbcast:2 row_mask:0xf bank_mask:0xf bound_ctrl:1
	v_mov_b32_dpp v31, v120 row_newbcast:3 row_mask:0xf bank_mask:0xf bound_ctrl:1
	v_mov_b32_dpp v29, v120 row_newbcast:4 row_mask:0xf bank_mask:0xf bound_ctrl:1
	v_mov_b32_dpp v26, v120 row_newbcast:5 row_mask:0xf bank_mask:0xf bound_ctrl:1
	v_mov_b32_dpp v30, v120 row_newbcast:6 row_mask:0xf bank_mask:0xf bound_ctrl:1
	v_mov_b32_dpp v28, v120 row_newbcast:7 row_mask:0xf bank_mask:0xf bound_ctrl:1
	v_mov_b32_dpp v21, v120 row_newbcast:8 row_mask:0xf bank_mask:0xf bound_ctrl:1
	v_mov_b32_dpp v18, v32 quad_perm:[0,0,0,0] row_mask:0xf bank_mask:0xf bound_ctrl:1
	v_mov_b32_dpp v33, v32 quad_perm:[1,1,1,1] row_mask:0xf bank_mask:0xf bound_ctrl:1
	v_mov_b32_dpp v32, v32 quad_perm:[2,2,2,2] row_mask:0xf bank_mask:0xf bound_ctrl:1
	s_and_b64 s[12:13], vcc, s[4:5]
	s_and_b64 exec, exec, s[12:13]
	s_cbranch_execz .LBB1_39
	v_mul_f32_e32 v31, v31, v33
	v_fmac_f32_e32 v31, v27, v18
	v_mul_f32_e32 v27, v29, v33
	v_fmac_f32_e32 v27, v20, v18
	v_fmac_f32_e32 v27, v28, v32
	v_mul_f32_e32 v20, v26, v33
	v_fmac_f32_e32 v31, v30, v32
	v_fmac_f32_e32 v20, v19, v18
	v_mul_f32_e32 v18, v27, v27
	v_fmac_f32_e32 v20, v21, v32
	v_fmac_f32_e32 v18, v31, v31
	v_fmac_f32_e32 v18, v20, v20
	v_mad_u32_u24 v26, v56, 3, v57
	v_sqrt_f32_e32 v18, v18
	v_cndmask_b32_e64 v19, v20, v27, s[10:11]
	v_add_u32_e32 v29, 56, v26
	v_add_f32_e32 v21, 0x38d1b717, v18
	v_rcp_f32_e32 v21, v21
	v_cndmask_b32_e64 v20, v19, v31, s[8:9]
	v_mul_u32_u24_e32 v28, 0x2493, v26
	v_mul_u32_u24_e32 v30, 0x2493, v29
	v_lshrrev_b32_e32 v28, 16, v28
	v_lshrrev_b32_e32 v30, 16, v30
	v_mul_u32_u24_e32 v28, 66, v28
	v_mul_u32_u24_e32 v30, 66, v30
	v_lshl_add_u32 v28, v26, 1, v28
	v_lshl_add_u32 v30, v29, 1, v30
	v_cvt_f16_f32_e32 v27, v20
	v_fma_mixlo_f16 v20, v20, v21, 0
	ds_write_b16 v28, v27 offset:14368
	ds_write_b16 v30, v20 offset:14368
	s_and_b64 exec, exec, s[8:9]
	s_cbranch_execz .LBB1_39
	v_cmp_lt_u32_e32 vcc, 6, v56
	v_cvt_f16_f32_e32 v18, v18
	v_lshlrev_b32_e32 v19, 1, v56
	v_mov_b32_e32 v20, 0x42
	v_cndmask_b32_e32 v20, 0, v20, vcc
	v_add_u32_e32 v19, v19, v20
	ds_write_b16 v19, v18 offset:14848

.LBB1_41:
	s_or_b64 exec, exec, s[0:1]
	v_bfe_u32 v41, s3, v56, 1
	v_mov_b32_e32 v40, v254
	v_cvt_f32_u32_e32 v41, v41
	s_waitcnt lgkmcnt(0)
	s_barrier
	ds_read_b128 v[18:21], v252 offset:14336
	s_waitcnt vmcnt(4) lgkmcnt(0)
	v_mfma_f32_16x16x32_f16 v[14:17], v[18:21], v[124:127], 0
	v_mfma_f32_16x16x32_f16 v[6:9], v[18:21], v[128:131], 0
	s_nop 6
	ds_write2st64_b32 v253, v14, v15 offset1:2
	ds_write2st64_b32 v253, v16, v17 offset0:4 offset1:6
	ds_write2st64_b32 v253, v6, v7 offset0:1 offset1:3
	ds_write2st64_b32 v253, v8, v9 offset0:5 offset1:7
	s_waitcnt lgkmcnt(0)
	s_barrier
	s_and_saveexec_b64 s[0:1], s[4:5]
	s_cbranch_execz .LBB1_53
	ds_read_b128 v[14:17], v255
	ds_read_b128 v[6:9], v255 offset:256
	ds_read_b128 v[24:27], v54 offset:15616
	ds_read_b128 v[28:31], v54 offset:15872
	ds_read_b128 v[32:35], v54 offset:16128
	ds_read_b128 v[36:39], v54 offset:16384
	s_waitcnt vmcnt(0) lgkmcnt(4)
	v_pk_fma_f32 v[136:137], v[14:15], v[40:41], v[136:137] op_sel:[0,1,0]
	v_pk_fma_f32 v[138:139], v[16:17], v[40:41], v[138:139] op_sel:[0,1,0]
	v_pk_fma_f32 v[140:141], v[6:7], v[40:41], v[140:141] op_sel:[0,1,0]
	v_pk_fma_f32 v[142:143], v[8:9], v[40:41], v[142:143] op_sel:[0,1,0]
	v_pk_add_f32 v[10:11], v[136:137], v[138:139]
	v_pk_add_f32 v[12:13], v[140:141], v[142:143]
	v_mov_b32_e32 v15, 0x3727c5ac
	v_pk_add_f32 v[10:11], v[10:11], v[12:13]
	s_nop 0
	v_add_f32_e32 v10, v10, v11
	s_nop 1
	v_add_f32_dpp v10, v10, v10 quad_perm:[1,0,3,2] row_mask:0xf bank_mask:0xf bound_ctrl:1
	s_nop 1
	v_add_f32_dpp v10, v10, v10 quad_perm:[2,3,0,1] row_mask:0xf bank_mask:0xf bound_ctrl:1
	s_nop 1
	v_add_f32_dpp v10, v10, v10 row_half_mirror row_mask:0xf bank_mask:0xf bound_ctrl:1
	s_nop 1
	v_add_f32_dpp v10, v10, v10 row_mirror row_mask:0xf bank_mask:0xf bound_ctrl:1
	v_mul_f32_e32 v10, 0x3c000000, v10
	v_pk_add_f32 v[136:137], v[136:137], v[10:11] op_sel_hi:[1,0] neg_lo:[0,1] neg_hi:[0,1]
	v_pk_add_f32 v[138:139], v[138:139], v[10:11] op_sel_hi:[1,0] neg_lo:[0,1] neg_hi:[0,1]
	v_pk_add_f32 v[140:141], v[140:141], v[10:11] op_sel_hi:[1,0] neg_lo:[0,1] neg_hi:[0,1]
	v_pk_add_f32 v[142:143], v[142:143], v[10:11] op_sel_hi:[1,0] neg_lo:[0,1] neg_hi:[0,1]
	v_pk_mul_f32 v[12:13], v[136:137], v[136:137]
	v_pk_mul_f32 v[16:17], v[138:139], v[138:139]
	v_pk_fma_f32 v[12:13], v[140:141], v[140:141], v[12:13]
	v_pk_fma_f32 v[16:17], v[142:143], v[142:143], v[16:17]
	s_nop 0
	v_pk_add_f32 v[12:13], v[12:13], v[16:17]
	s_nop 0
	v_add_f32_e32 v12, v12, v13
	s_nop 1
	v_add_f32_dpp v12, v12, v12 quad_perm:[1,0,3,2] row_mask:0xf bank_mask:0xf bound_ctrl:1
	s_nop 1
	v_add_f32_dpp v12, v12, v12 quad_perm:[2,3,0,1] row_mask:0xf bank_mask:0xf bound_ctrl:1
	s_nop 1
	v_add_f32_dpp v12, v12, v12 row_half_mirror row_mask:0xf bank_mask:0xf bound_ctrl:1
	s_nop 1
	v_add_f32_dpp v12, v12, v12 row_mirror row_mask:0xf bank_mask:0xf bound_ctrl:1
	v_fmac_f32_e32 v15, 0x3c000000, v12
	v_rsq_f32_e32 v14, v15
	s_nop 0
	v_pk_mul_f32 v[136:137], v[136:137], v[14:15] op_sel_hi:[1,0]
	v_pk_mul_f32 v[138:139], v[138:139], v[14:15] op_sel_hi:[1,0]
	v_pk_mul_f32 v[140:141], v[140:141], v[14:15] op_sel_hi:[1,0]
	v_pk_mul_f32 v[142:143], v[142:143], v[14:15] op_sel_hi:[1,0]
	s_waitcnt lgkmcnt(0)
	v_pk_fma_f32 v[136:137], v[24:25], v[136:137], v[32:33]
	v_pk_fma_f32 v[138:139], v[26:27], v[138:139], v[34:35]
	v_pk_fma_f32 v[140:141], v[28:29], v[140:141], v[36:37]
	v_pk_fma_f32 v[142:143], v[30:31], v[142:143], v[38:39]
	global_store_dwordx4 v40, v[136:139], s[14:15] nt
	global_store_dwordx4 v40, v[140:143], s[14:15] offset:256 nt

	.amdhsa_kernel _Z11attn_kernelILi4EEvPKfS1_S1_S1_S1_S1_PKcPf
		.amdhsa_group_segment_fixed_size 16640
		.amdhsa_private_segment_fixed_size 0
		.amdhsa_kernarg_size 64
		.amdhsa_user_sgpr_count 2
		.amdhsa_user_sgpr_dispatch_ptr 0
		.amdhsa_user_sgpr_queue_ptr 0
		.amdhsa_user_sgpr_kernarg_segment_ptr 1
		.amdhsa_user_sgpr_dispatch_id 0
		.amdhsa_user_sgpr_kernarg_preload_length 0
		.amdhsa_user_sgpr_kernarg_preload_offset 0
		.amdhsa_user_sgpr_private_segment_size 0
		.amdhsa_uses_dynamic_stack 0
		.amdhsa_enable_private_segment 0
		.amdhsa_system_sgpr_workgroup_id_x 1
		.amdhsa_system_sgpr_workgroup_id_y 0
		.amdhsa_system_sgpr_workgroup_id_z 0
		.amdhsa_system_sgpr_workgroup_info 0
		.amdhsa_system_vgpr_workitem_id 0
		.amdhsa_next_free_vgpr 256
		.amdhsa_next_free_sgpr 32
		.amdhsa_accum_offset 256
		.amdhsa_reserve_vcc 1
		.amdhsa_float_round_mode_32 0
		.amdhsa_float_round_mode_16_64 0
		.amdhsa_float_denorm_mode_32 3
		.amdhsa_float_denorm_mode_16_64 3
		.amdhsa_dx10_clamp 1
		.amdhsa_ieee_mode 1
		.amdhsa_fp16_overflow 0
		.amdhsa_tg_split 0
		.amdhsa_exception_fp_ieee_invalid_op 0
		.amdhsa_exception_fp_denorm_src 0
		.amdhsa_exception_fp_ieee_div_zero 0
		.amdhsa_exception_fp_ieee_overflow 0
		.amdhsa_exception_fp_ieee_underflow 0
		.amdhsa_exception_fp_ieee_inexact 0
		.amdhsa_exception_int_div_zero 0
	.end_amdhsa_kernel

amdhsa.kernels:
  - .agpr_count:     0
    .args:
      - .actual_access:  read_only
        .address_space:  global
        .offset:         0
        .size:           8
        .value_kind:     global_buffer
      - .actual_access:  read_only
        .address_space:  global
        .offset:         8
        .size:           8
        .value_kind:     global_buffer
      - .actual_access:  read_only
        .address_space:  global
        .offset:         16
        .size:           8
        .value_kind:     global_buffer
      - .actual_access:  read_only
        .address_space:  global
        .offset:         24
        .size:           8
        .value_kind:     global_buffer
      - .actual_access:  read_only
        .address_space:  global
        .offset:         32
        .size:           8
        .value_kind:     global_buffer
      - .actual_access:  read_only
        .address_space:  global
        .offset:         40
        .size:           8
        .value_kind:     global_buffer
      - .actual_access:  read_only
        .address_space:  global
        .offset:         48
        .size:           8
        .value_kind:     global_buffer
      - .actual_access:  read_only
        .address_space:  global
        .offset:         56
        .size:           8
        .value_kind:     global_buffer
      - .actual_access:  read_only
        .address_space:  global
        .offset:         64
        .size:           8
        .value_kind:     global_buffer
      - .actual_access:  read_only
        .address_space:  global
        .offset:         72
        .size:           8
        .value_kind:     global_buffer
      - .actual_access:  write_only
        .address_space:  global
        .offset:         80
        .size:           8
        .value_kind:     global_buffer
    .group_segment_fixed_size: 13056
    .kernarg_segment_align: 8
    .kernarg_segment_size: 88
    .language:       OpenCL C
    .language_version:
      - 2
      - 0
    .max_flat_workgroup_size: 128
    .name:           _Z11prep_kernelPKfS0_PKiS2_S0_S0_S0_S0_S0_S0_Pc
    .private_segment_fixed_size: 0
    .sgpr_count:     38
    .sgpr_spill_count: 0
    .symbol:         _Z11prep_kernelPKfS0_PKiS2_S0_S0_S0_S0_S0_S0_Pc.kd
    .uniform_work_group_size: 1
    .uses_dynamic_stack: false
    .vgpr_count:     144
    .vgpr_spill_count: 0
    .wavefront_size: 64
  - .agpr_count:     0
    .args:
      - .actual_access:  read_only
        .address_space:  global
        .offset:         0
        .size:           8
        .value_kind:     global_buffer
      - .actual_access:  read_only
        .address_space:  global
        .offset:         8
        .size:           8
        .value_kind:     global_buffer
      - .actual_access:  read_only
        .address_space:  global
        .offset:         16
        .size:           8
        .value_kind:     global_buffer
      - .actual_access:  read_only
        .address_space:  global
        .offset:         24
        .size:           8
        .value_kind:     global_buffer
      - .actual_access:  read_only
        .address_space:  global
        .offset:         32
        .size:           8
        .value_kind:     global_buffer
      - .actual_access:  read_only
        .address_space:  global
        .offset:         40
        .size:           8
        .value_kind:     global_buffer
      - .actual_access:  read_only
        .address_space:  global
        .offset:         48
        .size:           8
        .value_kind:     global_buffer
      - .actual_access:  write_only
        .address_space:  global
        .offset:         56
        .size:           8
        .value_kind:     global_buffer
    .group_segment_fixed_size: 16640
    .kernarg_segment_align: 8
    .kernarg_segment_size: 64
    .language:       OpenCL C
    .language_version:
      - 2
      - 0
    .max_flat_workgroup_size: 256
    .name:           _Z11attn_kernelILi4EEvPKfS1_S1_S1_S1_S1_PKcPf
    .private_segment_fixed_size: 0
    .sgpr_count:     38
    .sgpr_spill_count: 0
    .symbol:         _Z11attn_kernelILi4EEvPKfS1_S1_S1_S1_S1_PKcPf.kd
    .uniform_work_group_size: 1
    .uses_dynamic_stack: false
    .vgpr_count:     256
    .vgpr_spill_count: 0
    .wavefront_size: 64
